# prep: conversion blocks start ~0.5us later (s_sleep) so the weight-folding loads reach memory first
# speedup vs baseline: 1.0067x; 1.0067x over previous
.LBB0_39:
	s_sleep 16
	s_load_dwordx4 s[4:7], s[0:1], 0x28
	s_lshl_b32 s0, s2, 3
	s_bfe_u32 s3, s2, 0x20001
	s_and_b32 s1, s0, 8
	s_lshr_b32 s2, s2, 5
	s_or_b32 s2, s1, s2
	s_lshl_b32 s1, s3, 8
	s_and_b32 s9, s0, 0xc0
	v_and_b32_e32 v76, 56, v0
	s_or_b32 s0, s1, s9
	v_or_b32_e32 v1, s0, v76
	v_lshlrev_b32_e32 v70, 14, v1
	v_lshlrev_b32_e32 v1, 2, v0
	s_movk_i32 s8, 0xc0
	v_mov_b32_e32 v71, 0
	v_and_b32_e32 v1, 28, v1
	s_mov_b32 s1, 0
	s_waitcnt lgkmcnt(0)
	v_lshl_add_u64 v[2:3], s[4:5], 0, v[70:71]
	s_lshl_b32 s0, s2, 8
	v_and_or_b32 v77, v0, s8, v1
	v_lshl_add_u64 v[2:3], s[0:1], 2, v[2:3]
	v_lshlrev_b32_e32 v70, 2, v77
	v_lshl_add_u64 v[56:57], v[2:3], 0, v[70:71]
	s_mov_b32 s0, 0x18000
	v_add_co_u32_e32 v58, vcc, s0, v56
	s_mov_b32 s0, 0x1c000
	s_nop 0
	v_addc_co_u32_e32 v59, vcc, 0, v57, vcc
	v_add_co_u32_e32 v60, vcc, s0, v56
	s_mov_b32 s1, 0x10000
	s_nop 0
	v_addc_co_u32_e32 v61, vcc, 0, v57, vcc
	v_add_co_u32_e32 v62, vcc, s1, v56
	s_mov_b32 s4, 0x14000
	s_nop 0
	v_addc_co_u32_e32 v63, vcc, 0, v57, vcc
	v_add_co_u32_e32 v64, vcc, s4, v56
	s_mov_b32 s0, 0x8000
	s_nop 0
	v_addc_co_u32_e32 v65, vcc, 0, v57, vcc
	v_add_co_u32_e32 v66, vcc, s0, v56
	s_mov_b32 s5, 0xc000
	s_nop 0
	v_addc_co_u32_e32 v67, vcc, 0, v57, vcc
	global_load_dwordx4 v[0:3], v[58:59], off nt
	global_load_dwordx4 v[4:7], v[60:61], off nt
	v_add_co_u32_e32 v72, vcc, s5, v56
	global_load_dwordx4 v[8:11], v[62:63], off nt
	global_load_dwordx4 v[12:15], v[64:65], off nt
	s_movk_i32 s8, 0x4000
	v_addc_co_u32_e32 v73, vcc, 0, v57, vcc
	v_add_co_u32_e32 v74, vcc, s8, v56
	s_lshl_b32 s0, s3, 21
	s_nop 0
	v_addc_co_u32_e32 v75, vcc, 0, v57, vcc
	global_load_dwordx4 v[16:19], v[66:67], off nt
	global_load_dwordx4 v[20:23], v[72:73], off nt
	global_load_dwordx4 v[24:27], v[74:75], off nt
	global_load_dwordx4 v[28:31], v[56:57], off nt
	global_load_dwordx4 v[32:35], v[56:57], off offset:128 nt
	global_load_dwordx4 v[36:39], v[58:59], off offset:128 nt
	global_load_dwordx4 v[40:43], v[60:61], off offset:128 nt
	global_load_dwordx4 v[44:47], v[62:63], off offset:128 nt
	global_load_dwordx4 v[48:51], v[64:65], off offset:128 nt
	global_load_dwordx4 v[52:55], v[66:67], off offset:128 nt
	s_nop 0
	global_load_dwordx4 v[62:65], v[72:73], off offset:128 nt
	global_load_dwordx4 v[66:69], v[74:75], off offset:128 nt
	s_lshl_b32 s1, s2, 17
	s_or_b32 s0, s1, s0
	s_add_u32 s0, s6, s0
	s_addc_u32 s1, s7, 0
	s_lshl_b32 s2, s9, 1
	s_add_u32 s0, s0, s2
	v_lshlrev_b32_e32 v70, 1, v76
	s_addc_u32 s1, s1, 0
	s_waitcnt vmcnt(14)
	v_cvt_pk_f16_f32 v59, v0, v4
	v_cvt_pk_f16_f32 v5, v1, v5
	v_cvt_pk_f16_f32 v61, v2, v6
	s_waitcnt vmcnt(12)
	v_cvt_pk_f16_f32 v58, v8, v12
	v_cvt_pk_f16_f32 v4, v9, v13
	v_lshl_add_u64 v[8:9], s[0:1], 0, v[70:71]
	v_lshlrev_b32_e32 v70, 9, v77
	v_cvt_pk_f16_f32 v7, v3, v7
	v_cvt_pk_f16_f32 v60, v10, v14
	v_cvt_pk_f16_f32 v6, v11, v15
	v_lshl_add_u64 v[10:11], v[8:9], 0, v[70:71]
	s_waitcnt vmcnt(10)
	v_cvt_pk_f16_f32 v3, v17, v21
	s_waitcnt vmcnt(8)
	v_cvt_pk_f16_f32 v2, v29, v25
	global_store_dwordx4 v[10:11], v[2:5], off offset:512
	v_or_b32_e32 v70, 0x4000, v70
	s_waitcnt vmcnt(2)
	v_cvt_pk_f16_f32 v1, v52, v62
	v_cvt_pk_f16_f32 v5, v19, v23
	v_cvt_pk_f16_f32 v4, v31, v27
	global_store_dwordx4 v[10:11], v[4:7], off offset:1536
	v_cvt_pk_f16_f32 v3, v36, v40
	v_cvt_pk_f16_f32 v2, v44, v48
	s_waitcnt vmcnt(2)
	v_cvt_pk_f16_f32 v0, v32, v66
	v_lshl_add_u64 v[4:5], v[8:9], 0, v[70:71]
	global_store_dwordx4 v[4:5], v[0:3], off
	v_add_co_u32_e32 v4, vcc, s8, v10
	s_nop 0
	v_cvt_pk_f16_f32 v3, v37, v41
	v_cvt_pk_f16_f32 v2, v45, v49
	v_cvt_pk_f16_f32 v1, v53, v63
	v_cvt_pk_f16_f32 v0, v33, v67
	v_addc_co_u32_e32 v5, vcc, 0, v11, vcc
	v_cvt_pk_f16_f32 v57, v16, v20
	v_cvt_pk_f16_f32 v56, v28, v24
	global_store_dwordx4 v[4:5], v[0:3], off offset:512
	global_store_dwordx4 v[10:11], v[56:59], off
	s_nop 0
	v_cvt_pk_f16_f32 v3, v38, v42
	v_cvt_pk_f16_f32 v2, v46, v50
	v_cvt_pk_f16_f32 v1, v54, v64
	v_cvt_pk_f16_f32 v0, v34, v68
	v_cvt_pk_f16_f32 v59, v18, v22
	v_cvt_pk_f16_f32 v58, v30, v26
	global_store_dwordx4 v[4:5], v[0:3], off offset:1024
	global_store_dwordx4 v[10:11], v[58:61], off offset:1024
	s_nop 0
	v_cvt_pk_f16_f32 v3, v39, v43
	v_cvt_pk_f16_f32 v2, v47, v51
	v_cvt_pk_f16_f32 v1, v55, v65
	v_cvt_pk_f16_f32 v0, v35, v69
	global_store_dwordx4 v[4:5], v[0:3], off offset:1536
	s_endpgm
